# speedup vs baseline: 1.0151x; 1.0151x over previous
_Z9qsim_mainPKDF16_PK15HIP_vector_typeIfLj2EEPf:
	s_cmpk_gt_i32 s2, 0x3ff
	s_cbranch_scc1 .LBB1_11
	s_load_dwordx4 s[8:11], s[0:1], 0x0
	s_load_dwordx2 s[4:5], s[0:1], 0x10
	s_mul_i32 s1, s2, 56
	s_mul_hi_i32 s0, s2, 56
	v_mbcnt_lo_u32_b32 v2, -1, 0
	s_waitcnt lgkmcnt(0)
	s_add_u32 s6, s8, 0x20000
	s_addc_u32 s7, s9, 0
	s_add_u32 s20, s8, 0x80000
	s_addc_u32 s21, s9, 0
	s_add_u32 s12, s8, 0x38000
	s_addc_u32 s13, s9, 0
	s_add_i32 s22, s2, 0xfffffe00
	s_add_u32 s14, s4, s1
	s_addc_u32 s15, s5, s0
	s_mul_hi_i32 s0, s2, 0xa00
	s_mulk_i32 s2, 0xa00
	v_mbcnt_hi_u32_b32 v161, -1, v2
	s_add_u32 s10, s10, s2
	v_and_b32_e32 v2, 64, v161
	s_addc_u32 s11, s11, s0
	v_mov_b32_e32 v155, 0
	s_movk_i32 s23, 0x1000
	s_mov_b64 s[16:17], 0x28000
	v_mov_b32_e32 v1, 0x10000
	s_movk_i32 s24, 0x100
	v_mov_b32_e32 v158, 0x60
	v_mov_b32_e32 v159, 0x280
	v_mov_b32_e32 v160, 0x1280
	s_mov_b64 s[18:19], 0x40000
	s_mov_b32 s25, 0x40000
	v_xor_b32_e32 v162, 32, v161
	v_add_u32_e32 v163, 64, v2
	v_xor_b32_e32 v164, 16, v161
	v_mov_b32_e32 v165, 0x10a00
	v_and_b32_e32 v2, 63, v0
	v_lshlrev_b32_e32 v2, 4, v2
	v_add_u32_e32 v3, 0x1000, v2
	global_load_dwordx4 v[222:225], v2, s[6:7]
	global_load_dwordx4 v[226:229], v2, s[6:7] offset:1024
	global_load_dwordx4 v[230:233], v2, s[6:7] offset:2048
	global_load_dwordx4 v[234:237], v2, s[6:7] offset:3072
	global_load_dwordx4 v[238:241], v3, s[6:7]
	global_load_dwordx4 v[242:245], v3, s[6:7] offset:1024
	global_load_dwordx4 v[246:249], v3, s[6:7] offset:2048
	global_load_dwordx4 v[250:253], v3, s[6:7] offset:3072
	s_branch .LBB1_3

.Lskip_stage0:
	s_ashr_i32 s2, s4, 6
	s_lshl_b32 s3, s2, 3
	s_and_b32 s5, s3, 8
	s_bfe_u32 s26, s2, 0x10001
	s_or_b32 s5, s26, s5
	s_lshl_b32 s26, s2, 9
	s_and_b32 s26, s26, 0x400
	s_lshl_b32 s5, s5, 4
	s_or_b32 s28, s5, s26
	v_lshrrev_b32_e32 v182, 5, v167
	v_bfe_u32 v2, v156, 4, 1
	v_bitop3_b32 v3, v182, v156, 1 bitop3:0x78
	v_lshlrev_b32_e32 v154, 2, v182
	v_xor_b32_e32 v3, v3, v2
	v_bitop3_b32 v4, v154, v156, 4 bitop3:0x78
	v_and_b32_e32 v5, 10, v156
	v_or3_b32 v3, v5, v4, v3
	s_lshl_b32 s5, s2, 4
	v_lshlrev_b32_e32 v3, 4, v3
	s_lshl_b32 s3, s2, 13
	s_and_b32 s29, s5, 16
	v_lshlrev_b32_e32 v170, 8, v182
	v_lshl_or_b32 v171, v2, 10, v3
	s_or_b32 s26, s29, s3
	v_bitop3_b32 v179, v171, s26, v170 bitop3:0x36
	s_or_b32 s5, s26, 0x280
	v_bitop3_b32 v178, v171, s5, v170 bitop3:0x36
	s_or_b32 s30, s3, 0x800
	s_or_b32 s33, s3, 0x1000
	s_or_b32 s29, s29, 64
	s_or_b32 s34, s29, s33
	v_bitop3_b32 v180, v171, s34, v170 bitop3:0x36
	s_or_b32 s29, s3, s29
	s_or_b32 s29, s29, 0x1280
	s_and_b32 s5, s2, 1
	s_lshl_b32 s31, s5, 4
	s_or_b32 s2, s31, s3
	v_bitop3_b32 v173, v171, s2, v170 bitop3:0x36
	v_bitop3_b32 v34, v156, 31, v156 bitop3:0xc
	v_lshrrev_b32_e32 v35, 4, v34
	v_bitop3_b32 v36, v34, v182, 1 bitop3:0x6c
	v_xor_b32_e32 v36, v36, v35
	v_bitop3_b32 v34, v34, v154, 4 bitop3:0x6c
	v_bitop3_b32 v37, v156, 10, 31 bitop3:8
	v_or3_b32 v34, v37, v34, v36
	v_lshlrev_b32_e32 v35, 10, v35
	v_lshlrev_b32_e32 v34, 4, v34
	v_or3_b32 v154, v35, v34, v170
	v_bitop3_b32 v172, s2, v154, v159 bitop3:0x36
	v_bitop3_b32 v176, v171, s29, v170 bitop3:0x36
	s_or_b32 s29, s31, s30
	s_or_b32 s29, s29, 0xa0
	v_bitop3_b32 v175, v171, s29, v170 bitop3:0x36
	s_or_b32 s29, s2, 0xaa0
	s_xor_b32 s29, s29, 0x80
	v_xor_b32_e32 v174, s29, v154
	s_or_b32 s29, s26, 0x18e0
	v_bitop3_b32 v181, v171, s29, v170 bitop3:0x36
	s_or_b32 s29, s26, 0x1a60
	v_bitop3_b32 v177, v171, s29, v170 bitop3:0x36
	s_or_b32 s29, s31, 64
	s_or_b32 s3, s3, s29
	s_mov_b32 s41, s3
	s_or_b32 s29, s29, s33
	s_mov_b32 s40, s29
	s_or_b32 s3, s2, 0x18e0
	s_mov_b32 s42, s3
	s_or_b32 s2, s2, 0x1ae0
	s_xor_b32 s2, s2, 0x80
	s_mov_b32 s43, s2
	s_lshr_b32 s38, s4, 1
	v_and_b32_e32 v26, 31, v167
	v_and_b32_e32 v27, 3, v167
	v_bfe_u32 v28, v167, 3, 1
	v_bfe_u32 v29, v167, 2, 1
	v_lshl_or_b32 v27, v28, 2, v27
	v_lshl_or_b32 v27, v29, 3, v27
	v_lshlrev_b32_e32 v32, 9, v182
	v_lshl_add_u32 v30, v27, 3, v32
	v_add_u32_e32 v30, 0x10000, v30
	v_lshl_add_u32 v31, v26, 3, v32
	v_add_u32_e32 v31, 0x10400, v31
	v_xor_b32_e32 v28, 31, v26
	v_lshl_add_u32 v28, v28, 3, v32
	v_add_u32_e32 v28, 0x10400, v28
	v_bfe_u32 v29, v167, 4, 1
	v_mul_u32_u24_e32 v29, 0x78, v29
	v_xor_b32_e32 v254, s38, v29
	v_or_b32_e32 v254, 0x10800, v254
	v_and_b32_e32 v33, 16, v167
	v_cmp_eq_u32_e32 vcc, 0, v33
	ds_read2_b64 v[66:69], v30 offset0:0 offset1:32
	ds_read2_b64 v[70:73], v30 offset0:16 offset1:48
	ds_read2_b64 v[198:201], v31 offset0:0 offset1:32
	ds_read2_b64 v[202:205], v28 offset0:0 offset1:32
	ds_read2_b64 v[206:209], v254 offset0:0 offset1:16
	ds_read2_b64 v[210:213], v254 offset0:32 offset1:48
	s_waitcnt lgkmcnt(0)
	v_cndmask_b32_e32 v74, v67, v66, vcc
	v_cndmask_b32_e32 v75, v69, v68, vcc
	v_cndmask_b32_e64 v76, v66, -v67, vcc
	v_cndmask_b32_e64 v77, v68, -v69, vcc
	v_cndmask_b32_e32 v78, v71, v70, vcc
	v_cndmask_b32_e32 v79, v73, v72, vcc
	v_cndmask_b32_e64 v80, v70, -v71, vcc
	v_cndmask_b32_e64 v81, v72, -v73, vcc
	v_cvt_pk_f16_f32 v190, v74, v75
	v_cvt_pk_f16_f32 v191, v74, v75
	v_cvt_pk_f16_f32 v192, v76, v77
	v_cvt_pk_f16_f32 v193, v76, v77
	v_cvt_pk_f16_f32 v194, v78, v79
	v_cvt_pk_f16_f32 v195, v78, v79
	v_cvt_pk_f16_f32 v196, v80, v81
	v_cvt_pk_f16_f32 v197, v80, v81
	v_mul_f32_e32 v66, v199, v207
	v_mul_f32_e32 v68, v199, v206
	v_mul_f32_e32 v67, v199, v209
	v_mul_f32_e32 v69, v199, v208
	v_fma_f32 v66, v198, v206, -v66
	v_fma_f32 v68, v198, v207, v68
	v_fma_f32 v67, v198, v208, -v67
	v_fma_f32 v69, v198, v209, v69
	v_cvt_pk_f16_f32 v214, v66, v67
	v_cvt_pk_f16_f32 v216, v68, v69
	v_mul_f32_e32 v70, v201, v211
	v_mul_f32_e32 v72, v201, v210
	v_mul_f32_e32 v71, v201, v213
	v_mul_f32_e32 v73, v201, v212
	v_fma_f32 v70, v200, v210, -v70
	v_fma_f32 v72, v200, v211, v72
	v_fma_f32 v71, v200, v212, -v71
	v_fma_f32 v73, v200, v213, v73
	v_cvt_pk_f16_f32 v215, v70, v71
	v_cvt_pk_f16_f32 v217, v72, v73
	v_mul_f32_e32 v66, v203, v207
	v_mul_f32_e32 v68, v203, v206
	v_mul_f32_e32 v67, v203, v209
	v_mul_f32_e32 v69, v203, v208
	v_fma_f32 v66, v202, v206, -v66
	v_fma_f32 v68, v202, v207, v68
	v_fma_f32 v67, v202, v208, -v67
	v_fma_f32 v69, v202, v209, v69
	v_cvt_pk_f16_f32 v218, v66, v67
	v_cvt_pk_f16_f32 v220, v68, v69
	v_mul_f32_e32 v70, v205, v211
	v_mul_f32_e32 v72, v205, v210
	v_mul_f32_e32 v71, v205, v213
	v_mul_f32_e32 v73, v205, v212
	v_fma_f32 v70, v204, v210, -v70
	v_fma_f32 v72, v204, v211, v72
	v_fma_f32 v71, v204, v212, -v71
	v_fma_f32 v73, v204, v213, v73
	v_cvt_pk_f16_f32 v219, v70, v71
	v_cvt_pk_f16_f32 v221, v72, v73
	v_xor_b32_e32 v255, 8, v254
	ds_read2_b64 v[206:209], v255 offset0:0 offset1:16
	ds_read2_b64 v[210:213], v255 offset0:32 offset1:48
	v_mfma_f32_32x32x16_f16 v[2:17], v[190:193], v[214:217], 0
	v_mfma_f32_32x32x16_f16 v[18:33], v[194:197], v[218:221], 0
	s_waitcnt lgkmcnt(0)
	v_mul_f32_e32 v66, v199, v207
	v_mul_f32_e32 v68, v199, v206
	v_mul_f32_e32 v67, v199, v209
	v_mul_f32_e32 v69, v199, v208
	v_fma_f32 v66, v198, v206, -v66
	v_fma_f32 v68, v198, v207, v68
	v_fma_f32 v67, v198, v208, -v67
	v_fma_f32 v69, v198, v209, v69
	v_cvt_pk_f16_f32 v214, v66, v67
	v_cvt_pk_f16_f32 v216, v68, v69
	v_mul_f32_e32 v70, v201, v211
	v_mul_f32_e32 v72, v201, v210
	v_mul_f32_e32 v71, v201, v213
	v_mul_f32_e32 v73, v201, v212
	v_fma_f32 v70, v200, v210, -v70
	v_fma_f32 v72, v200, v211, v72
	v_fma_f32 v71, v200, v212, -v71
	v_fma_f32 v73, v200, v213, v73
	v_cvt_pk_f16_f32 v215, v70, v71
	v_cvt_pk_f16_f32 v217, v72, v73
	v_cvt_pk_f16_f32 v2, v2, v3
	v_cvt_pk_f16_f32 v3, v4, v5
	v_cvt_pk_f16_f32 v4, v6, v7
	v_cvt_pk_f16_f32 v5, v8, v9
	v_cvt_pk_f16_f32 v6, v10, v11
	v_cvt_pk_f16_f32 v7, v12, v13
	v_cvt_pk_f16_f32 v8, v14, v15
	v_cvt_pk_f16_f32 v9, v16, v17
	v_cvt_pk_f16_f32 v18, v18, v19
	v_cvt_pk_f16_f32 v19, v20, v21
	v_cvt_pk_f16_f32 v20, v22, v23
	v_cvt_pk_f16_f32 v21, v24, v25
	v_cvt_pk_f16_f32 v22, v26, v27
	v_cvt_pk_f16_f32 v23, v28, v29
	v_cvt_pk_f16_f32 v24, v30, v31
	v_cvt_pk_f16_f32 v25, v32, v33
	s_setprio 1
	s_waitcnt vmcnt(6)
	v_mul_f32_e32 v66, v203, v207
	v_mul_f32_e32 v68, v203, v206
	v_mfma_f32_32x32x16_f16 v[34:49], v[2:5], v[150:153], 0
	v_mul_f32_e32 v67, v203, v209
	v_mul_f32_e32 v69, v203, v208
	v_mfma_f32_32x32x16_f16 v[34:49], v[18:21], v[146:149], v[34:49]
	v_fma_f32 v66, v202, v206, -v66
	v_fma_f32 v68, v202, v207, v68
	v_mfma_f32_32x32x16_f16 v[34:49], v[6:9], v[142:145], v[34:49]
	v_fma_f32 v67, v202, v208, -v67
	v_fma_f32 v69, v202, v209, v69
	v_mfma_f32_32x32x16_f16 v[34:49], v[22:25], v[138:141], v[34:49]
	v_cvt_pk_f16_f32 v218, v66, v67
	v_cvt_pk_f16_f32 v220, v68, v69
	s_waitcnt vmcnt(2)
	v_mul_f32_e32 v70, v205, v211
	v_mul_f32_e32 v72, v205, v210
	v_mfma_f32_32x32x16_f16 v[50:65], v[2:5], v[134:137], 0
	v_mul_f32_e32 v71, v205, v213
	v_mul_f32_e32 v73, v205, v212
	v_mfma_f32_32x32x16_f16 v[50:65], v[18:21], v[126:129], v[50:65]
	v_fma_f32 v70, v204, v210, -v70
	v_fma_f32 v72, v204, v211, v72
	v_mfma_f32_32x32x16_f16 v[50:65], v[6:9], v[122:125], v[50:65]
	v_fma_f32 v71, v204, v212, -v71
	v_fma_f32 v73, v204, v213, v73
	v_mfma_f32_32x32x16_f16 v[50:65], v[22:25], v[130:133], v[50:65]
	v_cvt_pk_f16_f32 v219, v70, v71
	v_cvt_pk_f16_f32 v221, v72, v73
	v_xor_b32_e32 v255, 16, v254
	ds_read2_b64 v[206:209], v255 offset0:0 offset1:16
	ds_read2_b64 v[210:213], v255 offset0:32 offset1:48
	v_mfma_f32_32x32x16_f16 v[2:17], v[190:193], v[214:217], 0
	v_mfma_f32_32x32x16_f16 v[18:33], v[194:197], v[218:221], 0
	v_cvt_pk_f16_f32 v34, v34, v35
	v_cvt_pk_f16_f32 v35, v36, v37
	v_cvt_pk_f16_f32 v36, v38, v39
	v_cvt_pk_f16_f32 v37, v40, v41
	v_cvt_pk_f16_f32 v38, v42, v43
	v_cvt_pk_f16_f32 v39, v44, v45
	v_cvt_pk_f16_f32 v40, v46, v47
	v_cvt_pk_f16_f32 v41, v48, v49
	v_cvt_pk_f16_f32 v50, v50, v51
	v_cvt_pk_f16_f32 v51, v52, v53
	v_cvt_pk_f16_f32 v52, v54, v55
	v_cvt_pk_f16_f32 v53, v56, v57
	v_cvt_pk_f16_f32 v54, v58, v59
	v_cvt_pk_f16_f32 v55, v60, v61
	v_cvt_pk_f16_f32 v56, v62, v63
	v_cvt_pk_f16_f32 v57, v64, v65
	s_waitcnt vmcnt(2)
	v_cvt_pk_f16_f32 v2, v2, v3
	v_cvt_pk_f16_f32 v3, v4, v5
	v_cvt_pk_f16_f32 v4, v6, v7
	v_cvt_pk_f16_f32 v5, v8, v9
	v_mfma_f32_32x32x16_f16 v[90:105], v[34:37], v[222:225], 0
	v_cvt_pk_f16_f32 v6, v10, v11
	v_cvt_pk_f16_f32 v7, v12, v13
	v_cvt_pk_f16_f32 v8, v14, v15
	v_cvt_pk_f16_f32 v9, v16, v17
	v_mfma_f32_32x32x16_f16 v[106:121], v[34:37], v[238:241], 0
	v_cvt_pk_f16_f32 v18, v18, v19
	v_cvt_pk_f16_f32 v19, v20, v21
	v_cvt_pk_f16_f32 v20, v22, v23
	v_cvt_pk_f16_f32 v21, v24, v25
	v_mfma_f32_32x32x16_f16 v[90:105], v[38:41], v[226:229], v[90:105]
	v_cvt_pk_f16_f32 v22, v26, v27
	v_cvt_pk_f16_f32 v23, v28, v29
	v_cvt_pk_f16_f32 v24, v30, v31
	v_cvt_pk_f16_f32 v25, v32, v33
	v_mfma_f32_32x32x16_f16 v[106:121], v[38:41], v[242:245], v[106:121]
	s_waitcnt lgkmcnt(0)
	v_mul_f32_e32 v66, v199, v207
	v_mul_f32_e32 v68, v199, v206
	v_mul_f32_e32 v67, v199, v209
	v_mfma_f32_32x32x16_f16 v[90:105], v[50:53], v[230:233], v[90:105]
	v_mul_f32_e32 v69, v199, v208
	v_fma_f32 v66, v198, v206, -v66
	v_fma_f32 v68, v198, v207, v68
	v_fma_f32 v67, v198, v208, -v67
	v_mfma_f32_32x32x16_f16 v[106:121], v[50:53], v[246:249], v[106:121]
	v_fma_f32 v69, v198, v209, v69
	v_cvt_pk_f16_f32 v214, v66, v67
	v_cvt_pk_f16_f32 v216, v68, v69
	v_mul_f32_e32 v70, v201, v211
	v_mfma_f32_32x32x16_f16 v[90:105], v[54:57], v[234:237], v[90:105]
	v_mul_f32_e32 v72, v201, v210
	v_mul_f32_e32 v71, v201, v213
	v_mul_f32_e32 v73, v201, v212
	v_fma_f32 v70, v200, v210, -v70
	v_mfma_f32_32x32x16_f16 v[106:121], v[54:57], v[250:253], v[106:121]
	v_fma_f32 v72, v200, v211, v72
	v_fma_f32 v71, v200, v212, -v71
	v_fma_f32 v73, v200, v213, v73
	v_cvt_pk_f16_f32 v215, v70, v71
	v_cvt_pk_f16_f32 v217, v72, v73
	v_mfma_f32_32x32x16_f16 v[34:49], v[2:5], v[150:153], 0
	v_mul_f32_e32 v66, v203, v207
	v_mul_f32_e32 v68, v203, v206
	v_mul_f32_e32 v67, v203, v209
	v_mul_f32_e32 v69, v203, v208
	v_fma_f32 v66, v202, v206, -v66
	v_mfma_f32_32x32x16_f16 v[34:49], v[18:21], v[146:149], v[34:49]
	v_fma_f32 v68, v202, v207, v68
	v_fma_f32 v67, v202, v208, -v67
	v_fma_f32 v69, v202, v209, v69
	v_cvt_pk_f16_f32 v218, v66, v67
	v_cvt_pk_f16_f32 v220, v68, v69
	v_mfma_f32_32x32x16_f16 v[34:49], v[6:9], v[142:145], v[34:49]
	v_mul_f32_e32 v70, v205, v211
	v_mul_f32_e32 v72, v205, v210
	v_mul_f32_e32 v71, v205, v213
	v_mul_f32_e32 v73, v205, v212
	v_fma_f32 v70, v204, v210, -v70
	v_mfma_f32_32x32x16_f16 v[34:49], v[22:25], v[138:141], v[34:49]
	v_fma_f32 v72, v204, v211, v72
	v_fma_f32 v71, v204, v212, -v71
	v_fma_f32 v73, v204, v213, v73
	v_cvt_pk_f16_f32 v219, v70, v71
	v_cvt_pk_f16_f32 v221, v72, v73
	v_mfma_f32_32x32x16_f16 v[50:65], v[2:5], v[134:137], 0
	v_cvt_pk_f16_f32 v90, v90, v91
	v_cvt_pk_f16_f32 v91, v92, v93
	v_cvt_pk_f16_f32 v92, v94, v95
	v_cvt_pk_f16_f32 v93, v96, v97
	v_cvt_pk_f16_f32 v94, v98, v99
	v_mfma_f32_32x32x16_f16 v[50:65], v[18:21], v[126:129], v[50:65]
	v_cvt_pk_f16_f32 v95, v100, v101
	v_cvt_pk_f16_f32 v96, v102, v103
	v_cvt_pk_f16_f32 v97, v104, v105
	v_cvt_pk_f16_f32 v106, v106, v107
	v_cvt_pk_f16_f32 v107, v108, v109
	v_mfma_f32_32x32x16_f16 v[50:65], v[6:9], v[122:125], v[50:65]
	v_cvt_pk_f16_f32 v108, v110, v111
	v_cvt_pk_f16_f32 v109, v112, v113
	v_cvt_pk_f16_f32 v110, v114, v115
	v_cvt_pk_f16_f32 v111, v116, v117
	v_cvt_pk_f16_f32 v112, v118, v119
	v_mfma_f32_32x32x16_f16 v[50:65], v[22:25], v[130:133], v[50:65]
	v_cvt_pk_f16_f32 v113, v120, v121
	ds_write_b128 v173, v[90:93]
	ds_write_b128 v172, v[94:97]
	ds_write_b128 v173, v[106:109] offset:32768
	ds_write_b128 v172, v[110:113] offset:32768
	v_xor_b32_e32 v255, 24, v254
	ds_read2_b64 v[206:209], v255 offset0:0 offset1:16
	ds_read2_b64 v[210:213], v255 offset0:32 offset1:48
	v_mfma_f32_32x32x16_f16 v[2:17], v[190:193], v[214:217], 0
	v_mfma_f32_32x32x16_f16 v[18:33], v[194:197], v[218:221], 0
	v_cvt_pk_f16_f32 v34, v34, v35
	v_cvt_pk_f16_f32 v35, v36, v37
	v_cvt_pk_f16_f32 v36, v38, v39
	v_cvt_pk_f16_f32 v37, v40, v41
	v_cvt_pk_f16_f32 v38, v42, v43
	v_cvt_pk_f16_f32 v39, v44, v45
	v_cvt_pk_f16_f32 v40, v46, v47
	v_cvt_pk_f16_f32 v41, v48, v49
	v_cvt_pk_f16_f32 v50, v50, v51
	v_cvt_pk_f16_f32 v51, v52, v53
	v_cvt_pk_f16_f32 v52, v54, v55
	v_cvt_pk_f16_f32 v53, v56, v57
	v_cvt_pk_f16_f32 v54, v58, v59
	v_cvt_pk_f16_f32 v55, v60, v61
	v_cvt_pk_f16_f32 v56, v62, v63
	v_cvt_pk_f16_f32 v57, v64, v65
	v_mfma_f32_32x32x16_f16 v[90:105], v[34:37], v[222:225], 0
	v_cvt_pk_f16_f32 v2, v2, v3
	v_cvt_pk_f16_f32 v3, v4, v5
	v_cvt_pk_f16_f32 v4, v6, v7
	v_cvt_pk_f16_f32 v5, v8, v9
	v_mfma_f32_32x32x16_f16 v[106:121], v[34:37], v[238:241], 0
	v_cvt_pk_f16_f32 v6, v10, v11
	v_cvt_pk_f16_f32 v7, v12, v13
	v_cvt_pk_f16_f32 v8, v14, v15
	v_cvt_pk_f16_f32 v9, v16, v17
	v_cvt_pk_f16_f32 v18, v18, v19
	v_mfma_f32_32x32x16_f16 v[90:105], v[38:41], v[226:229], v[90:105]
	v_cvt_pk_f16_f32 v19, v20, v21
	v_cvt_pk_f16_f32 v20, v22, v23
	v_cvt_pk_f16_f32 v21, v24, v25
	v_cvt_pk_f16_f32 v22, v26, v27
	v_mfma_f32_32x32x16_f16 v[106:121], v[38:41], v[242:245], v[106:121]
	v_cvt_pk_f16_f32 v23, v28, v29
	v_cvt_pk_f16_f32 v24, v30, v31
	v_cvt_pk_f16_f32 v25, v32, v33
	s_waitcnt lgkmcnt(0)
	v_mul_f32_e32 v66, v199, v207
	v_mfma_f32_32x32x16_f16 v[90:105], v[50:53], v[230:233], v[90:105]
	v_mul_f32_e32 v68, v199, v206
	v_mul_f32_e32 v67, v199, v209
	v_mul_f32_e32 v69, v199, v208
	v_fma_f32 v66, v198, v206, -v66
	v_fma_f32 v68, v198, v207, v68
	v_mfma_f32_32x32x16_f16 v[106:121], v[50:53], v[246:249], v[106:121]
	v_fma_f32 v67, v198, v208, -v67
	v_fma_f32 v69, v198, v209, v69
	v_cvt_pk_f16_f32 v214, v66, v67
	v_cvt_pk_f16_f32 v216, v68, v69
	v_mfma_f32_32x32x16_f16 v[90:105], v[54:57], v[234:237], v[90:105]
	v_mul_f32_e32 v70, v201, v211
	v_mul_f32_e32 v72, v201, v210
	v_mul_f32_e32 v71, v201, v213
	v_mul_f32_e32 v73, v201, v212
	v_fma_f32 v70, v200, v210, -v70
	v_mfma_f32_32x32x16_f16 v[106:121], v[54:57], v[250:253], v[106:121]
	v_fma_f32 v72, v200, v211, v72
	v_fma_f32 v71, v200, v212, -v71
	v_fma_f32 v73, v200, v213, v73
	v_cvt_pk_f16_f32 v215, v70, v71
	v_cvt_pk_f16_f32 v217, v72, v73
	v_mfma_f32_32x32x16_f16 v[34:49], v[2:5], v[150:153], 0
	v_mul_f32_e32 v66, v203, v207
	v_mul_f32_e32 v68, v203, v206
	v_mul_f32_e32 v67, v203, v209
	v_mul_f32_e32 v69, v203, v208
	v_fma_f32 v66, v202, v206, -v66
	v_mfma_f32_32x32x16_f16 v[34:49], v[18:21], v[146:149], v[34:49]
	v_fma_f32 v68, v202, v207, v68
	v_fma_f32 v67, v202, v208, -v67
	v_fma_f32 v69, v202, v209, v69
	v_cvt_pk_f16_f32 v218, v66, v67
	v_cvt_pk_f16_f32 v220, v68, v69
	v_mfma_f32_32x32x16_f16 v[34:49], v[6:9], v[142:145], v[34:49]
	v_mul_f32_e32 v70, v205, v211
	v_mul_f32_e32 v72, v205, v210
	v_mul_f32_e32 v71, v205, v213
	v_mul_f32_e32 v73, v205, v212
	v_fma_f32 v70, v204, v210, -v70
	v_mfma_f32_32x32x16_f16 v[34:49], v[22:25], v[138:141], v[34:49]
	v_fma_f32 v72, v204, v211, v72
	v_fma_f32 v71, v204, v212, -v71
	v_fma_f32 v73, v204, v213, v73
	v_cvt_pk_f16_f32 v219, v70, v71
	v_cvt_pk_f16_f32 v221, v72, v73
	v_cvt_pk_f16_f32 v90, v90, v91
	v_mfma_f32_32x32x16_f16 v[50:65], v[2:5], v[134:137], 0
	v_cvt_pk_f16_f32 v91, v92, v93
	v_cvt_pk_f16_f32 v92, v94, v95
	v_cvt_pk_f16_f32 v93, v96, v97
	v_cvt_pk_f16_f32 v94, v98, v99
	v_cvt_pk_f16_f32 v95, v100, v101
	v_mfma_f32_32x32x16_f16 v[50:65], v[18:21], v[126:129], v[50:65]
	v_cvt_pk_f16_f32 v96, v102, v103
	v_cvt_pk_f16_f32 v97, v104, v105
	v_cvt_pk_f16_f32 v106, v106, v107
	v_cvt_pk_f16_f32 v107, v108, v109
	v_cvt_pk_f16_f32 v108, v110, v111
	v_mfma_f32_32x32x16_f16 v[50:65], v[6:9], v[122:125], v[50:65]
	v_cvt_pk_f16_f32 v109, v112, v113
	v_cvt_pk_f16_f32 v110, v114, v115
	v_cvt_pk_f16_f32 v111, v116, v117
	v_cvt_pk_f16_f32 v112, v118, v119
	v_cvt_pk_f16_f32 v113, v120, v121
	v_mfma_f32_32x32x16_f16 v[50:65], v[22:25], v[130:133], v[50:65]
	v_xor_b32_e32 v74, 0x8a0, v173
	v_xor_b32_e32 v75, 0x8a0, v172
	ds_write_b128 v74, v[90:93]
	ds_write_b128 v75, v[94:97]
	ds_write_b128 v74, v[106:109] offset:32768
	ds_write_b128 v75, v[110:113] offset:32768
	s_nop 0
	v_mfma_f32_32x32x16_f16 v[2:17], v[190:193], v[214:217], 0
	v_mfma_f32_32x32x16_f16 v[18:33], v[194:197], v[218:221], 0
	v_cvt_pk_f16_f32 v34, v34, v35
	v_cvt_pk_f16_f32 v35, v36, v37
	v_cvt_pk_f16_f32 v36, v38, v39
	v_cvt_pk_f16_f32 v37, v40, v41
	v_cvt_pk_f16_f32 v38, v42, v43
	v_cvt_pk_f16_f32 v39, v44, v45
	v_cvt_pk_f16_f32 v40, v46, v47
	v_cvt_pk_f16_f32 v41, v48, v49
	v_cvt_pk_f16_f32 v50, v50, v51
	v_cvt_pk_f16_f32 v51, v52, v53
	v_cvt_pk_f16_f32 v52, v54, v55
	v_cvt_pk_f16_f32 v53, v56, v57
	v_cvt_pk_f16_f32 v54, v58, v59
	v_cvt_pk_f16_f32 v55, v60, v61
	v_cvt_pk_f16_f32 v56, v62, v63
	v_cvt_pk_f16_f32 v57, v64, v65
	v_mfma_f32_32x32x16_f16 v[90:105], v[34:37], v[222:225], 0
	v_cvt_pk_f16_f32 v2, v2, v3
	v_cvt_pk_f16_f32 v3, v4, v5
	v_mfma_f32_32x32x16_f16 v[106:121], v[34:37], v[238:241], 0
	v_cvt_pk_f16_f32 v4, v6, v7
	v_cvt_pk_f16_f32 v5, v8, v9
	v_mfma_f32_32x32x16_f16 v[90:105], v[38:41], v[226:229], v[90:105]
	v_cvt_pk_f16_f32 v6, v10, v11
	v_cvt_pk_f16_f32 v7, v12, v13
	v_mfma_f32_32x32x16_f16 v[106:121], v[38:41], v[242:245], v[106:121]
	v_cvt_pk_f16_f32 v8, v14, v15
	v_cvt_pk_f16_f32 v9, v16, v17
	v_mfma_f32_32x32x16_f16 v[90:105], v[50:53], v[230:233], v[90:105]
	v_cvt_pk_f16_f32 v18, v18, v19
	v_cvt_pk_f16_f32 v19, v20, v21
	v_mfma_f32_32x32x16_f16 v[106:121], v[50:53], v[246:249], v[106:121]
	v_cvt_pk_f16_f32 v20, v22, v23
	v_cvt_pk_f16_f32 v21, v24, v25
	v_mfma_f32_32x32x16_f16 v[90:105], v[54:57], v[234:237], v[90:105]
	v_cvt_pk_f16_f32 v22, v26, v27
	v_cvt_pk_f16_f32 v23, v28, v29
	v_mfma_f32_32x32x16_f16 v[106:121], v[54:57], v[250:253], v[106:121]
	v_cvt_pk_f16_f32 v24, v30, v31
	v_cvt_pk_f16_f32 v25, v32, v33
	v_mfma_f32_32x32x16_f16 v[34:49], v[2:5], v[150:153], 0
	v_mfma_f32_32x32x16_f16 v[34:49], v[18:21], v[146:149], v[34:49]
	v_mfma_f32_32x32x16_f16 v[34:49], v[6:9], v[142:145], v[34:49]
	v_mfma_f32_32x32x16_f16 v[34:49], v[22:25], v[138:141], v[34:49]
	v_mfma_f32_32x32x16_f16 v[50:65], v[2:5], v[134:137], 0
	s_nop 5
	v_cvt_pk_f16_f32 v90, v90, v91
	v_cvt_pk_f16_f32 v91, v92, v93
	v_cvt_pk_f16_f32 v92, v94, v95
	v_cvt_pk_f16_f32 v93, v96, v97
	v_mfma_f32_32x32x16_f16 v[50:65], v[18:21], v[126:129], v[50:65]
	v_cvt_pk_f16_f32 v94, v98, v99
	v_cvt_pk_f16_f32 v95, v100, v101
	v_cvt_pk_f16_f32 v96, v102, v103
	v_cvt_pk_f16_f32 v97, v104, v105
	v_cvt_pk_f16_f32 v106, v106, v107
	v_cvt_pk_f16_f32 v107, v108, v109
	v_mfma_f32_32x32x16_f16 v[50:65], v[6:9], v[122:125], v[50:65]
	v_cvt_pk_f16_f32 v108, v110, v111
	v_cvt_pk_f16_f32 v109, v112, v113
	v_cvt_pk_f16_f32 v110, v114, v115
	v_cvt_pk_f16_f32 v111, v116, v117
	v_cvt_pk_f16_f32 v112, v118, v119
	v_cvt_pk_f16_f32 v113, v120, v121
	v_mfma_f32_32x32x16_f16 v[50:65], v[22:25], v[130:133], v[50:65]
	v_xor_b32_e32 v74, 0x1040, v173
	v_xor_b32_e32 v75, 0x1040, v172
	ds_write_b128 v74, v[90:93]
	ds_write_b128 v75, v[94:97]
	ds_write_b128 v74, v[106:109] offset:32768
	ds_write_b128 v75, v[110:113] offset:32768
	s_nop 11
	v_cvt_pk_f16_f32 v34, v34, v35
	v_cvt_pk_f16_f32 v35, v36, v37
	v_cvt_pk_f16_f32 v36, v38, v39
	v_cvt_pk_f16_f32 v37, v40, v41
	v_cvt_pk_f16_f32 v38, v42, v43
	v_cvt_pk_f16_f32 v39, v44, v45
	v_cvt_pk_f16_f32 v40, v46, v47
	v_cvt_pk_f16_f32 v41, v48, v49
	v_cvt_pk_f16_f32 v50, v50, v51
	v_cvt_pk_f16_f32 v51, v52, v53
	v_cvt_pk_f16_f32 v52, v54, v55
	v_cvt_pk_f16_f32 v53, v56, v57
	v_cvt_pk_f16_f32 v54, v58, v59
	v_cvt_pk_f16_f32 v55, v60, v61
	v_cvt_pk_f16_f32 v56, v62, v63
	v_cvt_pk_f16_f32 v57, v64, v65
	v_mfma_f32_32x32x16_f16 v[90:105], v[34:37], v[222:225], 0
	v_mfma_f32_32x32x16_f16 v[106:121], v[34:37], v[238:241], 0
	v_mfma_f32_32x32x16_f16 v[90:105], v[38:41], v[226:229], v[90:105]
	v_mfma_f32_32x32x16_f16 v[106:121], v[38:41], v[242:245], v[106:121]
	v_mfma_f32_32x32x16_f16 v[90:105], v[50:53], v[230:233], v[90:105]
	v_mfma_f32_32x32x16_f16 v[106:121], v[50:53], v[246:249], v[106:121]
	v_mfma_f32_32x32x16_f16 v[90:105], v[54:57], v[234:237], v[90:105]
	v_mfma_f32_32x32x16_f16 v[106:121], v[54:57], v[250:253], v[106:121]
	v_and_b32_e32 v134, 1, v156
	v_bitop3_b32 v132, v171, s40, v170 bitop3:0x36
	v_bitop3_b32 v131, s41, v154, v160 bitop3:0x36
	v_bitop3_b32 v135, v171, s42, v170 bitop3:0x36
	v_xor_b32_e32 v133, s43, v154
	v_and_b32_e32 v130, 4, v156
	s_lshl_b32 s2, s27, 3
	s_lshl_b32 s3, s5, 2
	s_or_b32 s2, s3, s2
	s_ashr_i32 s3, s2, 31
	s_lshl_b64 s[2:3], s[2:3], 13
	s_add_u32 s2, s20, s2
	s_addc_u32 s3, s21, s3
	v_lshlrev_b32_e32 v154, 1, v169
	v_lshl_add_u64 v[2:3], s[2:3], 0, v[154:155]
	v_add_co_u32_e32 v2, vcc, s23, v2
	s_nop 1
	v_addc_co_u32_e32 v3, vcc, 0, v3, vcc
	v_cvt_pk_f16_f32 v90, v90, v91
	v_cvt_pk_f16_f32 v91, v92, v93
	v_cvt_pk_f16_f32 v92, v94, v95
	v_cvt_pk_f16_f32 v93, v96, v97
	v_cvt_pk_f16_f32 v94, v98, v99
	v_cvt_pk_f16_f32 v95, v100, v101
	v_cvt_pk_f16_f32 v96, v102, v103
	v_cvt_pk_f16_f32 v97, v104, v105
	v_cvt_pk_f16_f32 v106, v106, v107
	v_cvt_pk_f16_f32 v107, v108, v109
	v_cvt_pk_f16_f32 v108, v110, v111
	v_cvt_pk_f16_f32 v109, v112, v113
	v_cvt_pk_f16_f32 v110, v114, v115
	v_cvt_pk_f16_f32 v111, v116, v117
	v_cvt_pk_f16_f32 v112, v118, v119
	v_cvt_pk_f16_f32 v113, v120, v121
	v_xor_b32_e32 v74, 0x18e0, v173
	v_xor_b32_e32 v75, 0x18e0, v172
	ds_write_b128 v74, v[90:93]
	ds_write_b128 v75, v[94:97]
	ds_write_b128 v74, v[106:109] offset:32768
	ds_write_b128 v75, v[110:113] offset:32768
	s_setprio 0
	s_waitcnt lgkmcnt(0)
	s_barrier
	global_load_dwordx4 v[62:65], v154, s[2:3]
	global_load_dwordx4 v[46:49], v154, s[2:3] offset:1024
	global_load_dwordx4 v[42:45], v154, s[2:3] offset:2048
	global_load_dwordx4 v[38:41], v154, s[2:3] offset:3072
	global_load_dwordx4 v[54:57], v[2:3], off offset:1024
	global_load_dwordx4 v[50:53], v[2:3], off offset:2048
	v_lshl_add_u64 v[4:5], s[12:13], 0, v[154:155]
	global_load_dwordx4 v[126:129], v154, s[12:13]
	global_load_dwordx4 v[122:125], v154, s[12:13] offset:1024
	global_load_dwordx4 v[118:121], v154, s[12:13] offset:2048
	global_load_dwordx4 v[114:117], v154, s[12:13] offset:3072
	global_load_dwordx4 v[34:37], v168, s[2:3]
	global_load_dwordx4 v[110:113], v168, s[12:13]
	v_add_co_u32_e32 v4, vcc, s23, v4
	s_nop 1
	v_addc_co_u32_e32 v5, vcc, 0, v5, vcc
	global_load_dwordx4 v[58:61], v[2:3], off offset:3072
	global_load_dwordx4 v[106:109], v[4:5], off offset:1024
	global_load_dwordx4 v[94:97], v[4:5], off offset:2048
	global_load_dwordx4 v[90:93], v[4:5], off offset:3072
	v_bfrev_b32_e32 v3, v156
	v_lshlrev_b32_e32 v7, 5, v167
	v_lshlrev_b32_e32 v6, 9, v167
	v_and_b32_e32 v7, 0x200, v7
	v_lshlrev_b32_e32 v8, 8, v167
	v_lshrrev_b32_e32 v3, 27, v3
	v_lshrrev_b32_e32 v2, 2, v167
	v_lshrrev_b32_e32 v4, 4, v156
	v_xor_b32_e32 v5, v169, v156
	v_and_b32_e32 v6, 0x5800, v6
	v_and_b32_e32 v3, 8, v3
	v_and_or_b32 v7, v8, s24, v7
	v_lshrrev_b32_e32 v5, 1, v5
	v_xor_b32_e32 v4, v2, v4
	v_or3_b32 v3, v7, v6, v3
	v_bitop3_b32 v7, v2, v182, 1 bitop3:0x6c
	v_lshlrev_b32_e32 v2, 1, v167
	v_and_b32_e32 v5, 4, v5
	v_lshlrev_b32_e32 v4, 3, v4
	v_lshrrev_b32_e32 v6, 1, v167
	v_and_b32_e32 v2, 2, v2
	v_and_or_b32 v9, v169, 8, v2
	v_and_b32_e32 v2, 8, v4
	v_and_or_b32 v4, v6, 2, v5
	v_or3_b32 v2, v4, v2, v134
	v_lshlrev_b32_e32 v2, 4, v2
	v_bitop3_b32 v146, v3, s28, v2 bitop3:0x36
	v_xor_b32_e32 v8, v6, v182
	v_xor_b32_e32 v147, 0x2010, v146
	v_lshlrev_b32_e32 v8, 2, v8
	v_and_b32_e32 v8, 4, v8
	v_or3_b32 v6, v9, v7, v8
	v_lshlrev_b32_e32 v7, 11, v167
	v_and_b32_e32 v8, 0x7800, v7
	v_lshlrev_b32_e32 v6, 4, v6
	v_or3_b32 v22, v6, v8, v170
	v_and_b32_e32 v23, 0x8000, v7
	v_xor_b32_e32 v150, 16, v146
	v_xad_u32 v70, v22, s28, v23
	v_xor_b32_e32 v151, 0x2000, v146
	ds_read_b64_tr_b16 v[18:19], v146
	ds_read_b64_tr_b16 v[20:21], v147
	ds_read_b64_tr_b16 v[22:23], v146 offset:32768
	ds_read_b64_tr_b16 v[24:25], v147 offset:32768
	ds_read_b64_tr_b16 v[26:27], v150
	ds_read_b64_tr_b16 v[28:29], v151
	ds_read_b64_tr_b16 v[30:31], v150 offset:32768
	ds_read_b64_tr_b16 v[32:33], v151 offset:32768
	v_xor_b32_e32 v148, 32, v146
	v_xor_b32_e32 v149, 0x2030, v146
	v_xor_b32_e32 v144, 48, v146
	v_xor_b32_e32 v145, 0x2020, v146
	v_xor_b32_e32 v142, 64, v146
	v_xor_b32_e32 v143, 0x2050, v146
	v_xor_b32_e32 v140, 0x50, v146
	v_xor_b32_e32 v141, 0x2040, v146
	v_xor_b32_e32 v138, 0x60, v146
	v_xor_b32_e32 v139, 0x2070, v146
	v_xor_b32_e32 v136, 0x70, v146
	v_xor_b32_e32 v137, 0x2060, v146
	v_xor_b32_e32 v71, 0x60, v70
	s_lshl_b64 s[0:1], s[0:1], 13
	s_add_u32 s0, s8, s0
	s_addc_u32 s1, s9, s1
	s_waitcnt vmcnt(17) lgkmcnt(4)
	v_mfma_f32_32x32x16_f16 v[2:17], v[18:21], v[86:89], 0
	s_waitcnt vmcnt(16)
	v_mfma_f32_32x32x16_f16 v[2:17], v[22:25], v[82:85], v[2:17]
	ds_read_b64_tr_b16 v[206:207], v148
	ds_read_b64_tr_b16 v[208:209], v149
	ds_read_b64_tr_b16 v[210:211], v148 offset:32768
	ds_read_b64_tr_b16 v[212:213], v149 offset:32768
	s_waitcnt lgkmcnt(4)
	v_mfma_f32_32x32x16_f16 v[190:205], v[26:29], v[86:89], 0
	v_mfma_f32_32x32x16_f16 v[190:205], v[30:33], v[82:85], v[190:205]
	s_nop 4
	v_cvt_pk_f16_f32 v2, v2, v3
	v_cvt_pk_f16_f32 v3, v4, v5
	v_cvt_pk_f16_f32 v4, v6, v7
	v_cvt_pk_f16_f32 v5, v8, v9
	v_cvt_pk_f16_f32 v6, v10, v11
	v_cvt_pk_f16_f32 v7, v12, v13
	v_cvt_pk_f16_f32 v8, v14, v15
	v_cvt_pk_f16_f32 v9, v16, v17
	v_xor_b32_e32 v73, 0x280, v70
	ds_write_b128 v70, v[2:5]
	ds_write_b128 v73, v[6:9]
	ds_read_b64_tr_b16 v[18:19], v144
	ds_read_b64_tr_b16 v[20:21], v145
	ds_read_b64_tr_b16 v[22:23], v144 offset:32768
	ds_read_b64_tr_b16 v[24:25], v145 offset:32768
	s_waitcnt lgkmcnt(6)
	v_mfma_f32_32x32x16_f16 v[2:17], v[206:209], v[86:89], 0
	v_mfma_f32_32x32x16_f16 v[2:17], v[210:213], v[82:85], v[2:17]
	v_cvt_pk_f16_f32 v190, v190, v191
	v_cvt_pk_f16_f32 v191, v192, v193
	v_cvt_pk_f16_f32 v192, v194, v195
	v_cvt_pk_f16_f32 v193, v196, v197
	v_cvt_pk_f16_f32 v194, v198, v199
	v_cvt_pk_f16_f32 v195, v200, v201
	v_cvt_pk_f16_f32 v196, v202, v203
	v_cvt_pk_f16_f32 v197, v204, v205
	v_xor_b32_e32 v72, 16, v70
	v_xor_b32_e32 v73, 0x290, v70
	ds_write_b128 v72, v[190:193]
	ds_write_b128 v73, v[194:197]
	ds_read_b64_tr_b16 v[26:27], v142
	ds_read_b64_tr_b16 v[28:29], v143
	ds_read_b64_tr_b16 v[30:31], v142 offset:32768
	ds_read_b64_tr_b16 v[32:33], v143 offset:32768
	s_waitcnt lgkmcnt(6)
	v_mfma_f32_32x32x16_f16 v[190:205], v[18:21], v[86:89], 0
	v_mfma_f32_32x32x16_f16 v[190:205], v[22:25], v[82:85], v[190:205]
	v_cvt_pk_f16_f32 v2, v2, v3
	v_cvt_pk_f16_f32 v3, v4, v5
	v_cvt_pk_f16_f32 v4, v6, v7
	v_cvt_pk_f16_f32 v5, v8, v9
	v_cvt_pk_f16_f32 v6, v10, v11
	v_cvt_pk_f16_f32 v7, v12, v13
	v_cvt_pk_f16_f32 v8, v14, v15
	v_cvt_pk_f16_f32 v9, v16, v17
	v_xor_b32_e32 v72, 32, v70
	v_xor_b32_e32 v73, 0x2a0, v70
	ds_write_b128 v72, v[2:5]
	ds_write_b128 v73, v[6:9]
	ds_read_b64_tr_b16 v[206:207], v140
	ds_read_b64_tr_b16 v[208:209], v141
	ds_read_b64_tr_b16 v[210:211], v140 offset:32768
	ds_read_b64_tr_b16 v[212:213], v141 offset:32768
	s_waitcnt lgkmcnt(6)
	v_mfma_f32_32x32x16_f16 v[2:17], v[26:29], v[86:89], 0
	v_mfma_f32_32x32x16_f16 v[2:17], v[30:33], v[82:85], v[2:17]
	v_cvt_pk_f16_f32 v190, v190, v191
	v_cvt_pk_f16_f32 v191, v192, v193
	v_cvt_pk_f16_f32 v192, v194, v195
	v_cvt_pk_f16_f32 v193, v196, v197
	v_cvt_pk_f16_f32 v194, v198, v199
	v_cvt_pk_f16_f32 v195, v200, v201
	v_cvt_pk_f16_f32 v196, v202, v203
	v_cvt_pk_f16_f32 v197, v204, v205
	v_xor_b32_e32 v72, 48, v70
	v_xor_b32_e32 v73, 0x2b0, v70
	ds_write_b128 v72, v[190:193]
	ds_write_b128 v73, v[194:197]
	ds_read_b64_tr_b16 v[18:19], v138
	ds_read_b64_tr_b16 v[20:21], v139
	ds_read_b64_tr_b16 v[22:23], v138 offset:32768
	ds_read_b64_tr_b16 v[24:25], v139 offset:32768
	s_waitcnt lgkmcnt(6)
	v_mfma_f32_32x32x16_f16 v[190:205], v[206:209], v[86:89], 0
	v_mfma_f32_32x32x16_f16 v[190:205], v[210:213], v[82:85], v[190:205]
	v_cvt_pk_f16_f32 v2, v2, v3
	v_cvt_pk_f16_f32 v3, v4, v5
	v_cvt_pk_f16_f32 v4, v6, v7
	v_cvt_pk_f16_f32 v5, v8, v9
	v_cvt_pk_f16_f32 v6, v10, v11
	v_cvt_pk_f16_f32 v7, v12, v13
	v_cvt_pk_f16_f32 v8, v14, v15
	v_cvt_pk_f16_f32 v9, v16, v17
	v_xor_b32_e32 v72, 64, v70
	v_xor_b32_e32 v73, 0x2c0, v70
	ds_write_b128 v72, v[2:5]
	ds_write_b128 v73, v[6:9]
	ds_read_b64_tr_b16 v[26:27], v136
	ds_read_b64_tr_b16 v[28:29], v137
	ds_read_b64_tr_b16 v[30:31], v136 offset:32768
	ds_read_b64_tr_b16 v[32:33], v137 offset:32768
	s_waitcnt lgkmcnt(6)
	v_mfma_f32_32x32x16_f16 v[2:17], v[18:21], v[86:89], 0
	v_mfma_f32_32x32x16_f16 v[2:17], v[22:25], v[82:85], v[2:17]
	v_cvt_pk_f16_f32 v190, v190, v191
	v_cvt_pk_f16_f32 v191, v192, v193
	v_cvt_pk_f16_f32 v192, v194, v195
	v_cvt_pk_f16_f32 v193, v196, v197
	v_cvt_pk_f16_f32 v194, v198, v199
	v_cvt_pk_f16_f32 v195, v200, v201
	v_cvt_pk_f16_f32 v196, v202, v203
	v_cvt_pk_f16_f32 v197, v204, v205
	v_xor_b32_e32 v72, 0x50, v70
	v_xor_b32_e32 v73, 0x2d0, v70
	ds_write_b128 v72, v[190:193]
	ds_write_b128 v73, v[194:197]
	s_waitcnt lgkmcnt(2)
	v_mfma_f32_32x32x16_f16 v[190:205], v[26:29], v[86:89], 0
	v_mfma_f32_32x32x16_f16 v[190:205], v[30:33], v[82:85], v[190:205]
	v_cvt_pk_f16_f32 v2, v2, v3
	v_cvt_pk_f16_f32 v3, v4, v5
	v_cvt_pk_f16_f32 v4, v6, v7
	v_cvt_pk_f16_f32 v5, v8, v9
	v_cvt_pk_f16_f32 v6, v10, v11
	v_cvt_pk_f16_f32 v7, v12, v13
	v_cvt_pk_f16_f32 v8, v14, v15
	v_cvt_pk_f16_f32 v9, v16, v17
	v_xor_b32_e32 v72, 0x60, v70
	v_xor_b32_e32 v73, 0x2e0, v70
	ds_write_b128 v72, v[2:5]
	ds_write_b128 v73, v[6:9]
	v_cvt_pk_f16_f32 v190, v190, v191
	v_cvt_pk_f16_f32 v191, v192, v193
	v_cvt_pk_f16_f32 v192, v194, v195
	v_cvt_pk_f16_f32 v193, v196, v197
	v_cvt_pk_f16_f32 v194, v198, v199
	v_cvt_pk_f16_f32 v195, v200, v201
	v_cvt_pk_f16_f32 v196, v202, v203
	v_cvt_pk_f16_f32 v197, v204, v205
	v_xor_b32_e32 v72, 0x70, v70
	v_xor_b32_e32 v73, 0x2f0, v70
	ds_write_b128 v72, v[190:193]
	ds_write_b128 v73, v[194:197]
	v_lshl_add_u64 v[2:3], s[0:1], 0, v[154:155]
	v_lshl_add_u64 v[4:5], v[2:3], 0, s[18:19]
	v_add_co_u32_e32 v2, vcc, s25, v2
	s_waitcnt lgkmcnt(0)
	s_nop 0
	v_addc_co_u32_e32 v3, vcc, 0, v3, vcc
	s_barrier
	global_load_dwordx4 v[102:105], v[2:3], off
	global_load_dwordx4 v[98:101], v[4:5], off offset:1024
	s_setprio 1
	s_add_u32 s0, s2, 0x2000
	s_addc_u32 s1, s3, 0
	v_lshl_add_u64 v[2:3], s[0:1], 0, v[154:155]
	v_add_co_u32_e32 v2, vcc, s23, v2
	global_load_dwordx4 v[66:69], v154, s[0:1]
	global_load_dwordx4 v[70:73], v154, s[0:1] offset:1024
	global_load_dwordx4 v[74:77], v154, s[0:1] offset:2048
	global_load_dwordx4 v[78:81], v154, s[0:1] offset:3072
	v_addc_co_u32_e32 v3, vcc, 0, v3, vcc
	global_load_dwordx4 v[82:85], v168, s[0:1]
	global_load_dwordx4 v[86:89], v[2:3], off offset:1024
	global_load_dwordx4 v[182:185], v[2:3], off offset:2048
	global_load_dwordx4 v[186:189], v[2:3], off offset:3072
	ds_read_b128 v[18:21], v179
	ds_read_b128 v[22:25], v179 offset:32768
	ds_read_b128 v[26:29], v178
	ds_read_b128 v[30:33], v178 offset:32768
	s_add_u32 s0, s2, 0x6000
	s_addc_u32 s1, s3, 0
	s_waitcnt vmcnt(25) lgkmcnt(3)
	v_mfma_f32_32x32x16_f16 v[2:17], v[18:21], v[62:65], 0
	s_add_u32 s2, s2, 0x4000
	s_addc_u32 s3, s3, 0
	s_or_b32 s27, s26, 0x8a0
	s_or_b32 s26, s26, 0xa20
	s_waitcnt vmcnt(24) lgkmcnt(1)
	v_mfma_f32_32x32x16_f16 v[2:17], v[26:29], v[46:49], v[2:17]
	s_waitcnt vmcnt(23)
	v_mfma_f32_32x32x16_f16 v[2:17], v[22:25], v[42:45], v[2:17]
	s_waitcnt vmcnt(22) lgkmcnt(0)
	v_mfma_f32_32x32x16_f16 v[2:17], v[30:33], v[38:41], v[2:17]
	s_waitcnt vmcnt(15)
	v_mfma_f32_32x32x16_f16 v[34:49], v[18:21], v[34:37], 0
	s_nop 9
	v_cvt_pk_f16_f32 v9, v8, v9
	v_cvt_pk_f16_f32 v8, v6, v7
	v_cvt_pk_f16_f32 v7, v4, v5
	v_cvt_pk_f16_f32 v6, v2, v3
	v_cvt_pk_f16_f32 v5, v16, v17
	v_cvt_pk_f16_f32 v4, v14, v15
	v_cvt_pk_f16_f32 v3, v12, v13
	v_mfma_f32_32x32x16_f16 v[34:49], v[26:29], v[54:57], v[34:49]
	v_cvt_pk_f16_f32 v2, v10, v11
	v_mfma_f32_32x32x16_f16 v[34:49], v[22:25], v[50:53], v[34:49]
	s_waitcnt vmcnt(13)
	v_mfma_f32_32x32x16_f16 v[34:49], v[30:33], v[58:61], v[34:49]
	v_mfma_f32_32x32x16_f16 v[18:33], v[6:9], v[126:129], 0
	s_nop 10
	v_cvt_pk_f16_f32 v13, v40, v41
	v_cvt_pk_f16_f32 v12, v38, v39
	v_cvt_pk_f16_f32 v11, v36, v37
	v_cvt_pk_f16_f32 v10, v34, v35
	v_cvt_pk_f16_f32 v17, v48, v49
	v_cvt_pk_f16_f32 v16, v46, v47
	v_cvt_pk_f16_f32 v15, v44, v45
	v_mfma_f32_32x32x16_f16 v[50:65], v[6:9], v[110:113], 0
	v_bitop3_b32 v6, v171, s27, v170 bitop3:0x36
	v_cvt_pk_f16_f32 v14, v42, v43
	v_mfma_f32_32x32x16_f16 v[18:33], v[2:5], v[122:125], v[18:33]
	s_waitcnt vmcnt(12)
	v_mfma_f32_32x32x16_f16 v[50:65], v[2:5], v[106:109], v[50:65]
	ds_read_b128 v[2:5], v6
	ds_read_b128 v[6:9], v6 offset:32768
	v_mfma_f32_32x32x16_f16 v[18:33], v[10:13], v[118:121], v[18:33]
	s_waitcnt vmcnt(11)
	v_mfma_f32_32x32x16_f16 v[50:65], v[10:13], v[94:97], v[50:65]
	s_waitcnt vmcnt(7) lgkmcnt(1)
	v_mfma_f32_32x32x16_f16 v[34:49], v[2:5], v[66:69], 0
	v_mfma_f32_32x32x16_f16 v[18:33], v[14:17], v[114:117], v[18:33]
	v_mfma_f32_32x32x16_f16 v[50:65], v[14:17], v[90:93], v[50:65]
	v_bitop3_b32 v14, v171, s26, v170 bitop3:0x36
	ds_read_b128 v[10:13], v14
	ds_read_b128 v[14:17], v14 offset:32768
	s_nop 7
	v_cvt_pk_f16_f32 v25, v24, v25
	v_cvt_pk_f16_f32 v24, v22, v23
	v_cvt_pk_f16_f32 v23, v20, v21
	v_cvt_pk_f16_f32 v22, v18, v19
	v_cvt_pk_f16_f32 v21, v32, v33
	s_waitcnt vmcnt(6) lgkmcnt(1)
	v_mfma_f32_32x32x16_f16 v[34:49], v[10:13], v[70:73], v[34:49]
	v_cvt_pk_f16_f32 v20, v30, v31
	v_cvt_pk_f16_f32 v19, v28, v29
	v_cvt_pk_f16_f32 v18, v26, v27
	ds_write_b128 v173, v[22:25]
	ds_write_b128 v172, v[18:21]
	v_cvt_pk_f16_f32 v21, v56, v57
	v_cvt_pk_f16_f32 v20, v54, v55
	s_waitcnt vmcnt(5)
	v_mfma_f32_32x32x16_f16 v[34:49], v[6:9], v[74:77], v[34:49]
	v_cvt_pk_f16_f32 v19, v52, v53
	v_cvt_pk_f16_f32 v18, v50, v51
	ds_write_b128 v173, v[18:21] offset:32768
	v_cvt_pk_f16_f32 v21, v64, v65
	v_cvt_pk_f16_f32 v20, v62, v63
	v_cvt_pk_f16_f32 v19, v60, v61
	v_cvt_pk_f16_f32 v18, v58, v59
	s_waitcnt vmcnt(4) lgkmcnt(3)
	v_mfma_f32_32x32x16_f16 v[34:49], v[14:17], v[78:81], v[34:49]
	ds_write_b128 v172, v[18:21] offset:32768
	s_waitcnt vmcnt(3)
	v_mfma_f32_32x32x16_f16 v[66:81], v[2:5], v[82:85], 0
	s_nop 8
	v_cvt_pk_f16_f32 v41, v40, v41
	v_cvt_pk_f16_f32 v40, v38, v39
	v_cvt_pk_f16_f32 v39, v36, v37
	v_cvt_pk_f16_f32 v38, v34, v35
	v_cvt_pk_f16_f32 v85, v48, v49
	v_cvt_pk_f16_f32 v84, v46, v47
	v_cvt_pk_f16_f32 v83, v44, v45
	s_waitcnt vmcnt(2)
	v_mfma_f32_32x32x16_f16 v[66:81], v[10:13], v[86:89], v[66:81]
	v_cvt_pk_f16_f32 v82, v42, v43
	s_waitcnt vmcnt(1)
	v_mfma_f32_32x32x16_f16 v[66:81], v[6:9], v[182:185], v[66:81]
	s_waitcnt vmcnt(0)
	v_mfma_f32_32x32x16_f16 v[66:81], v[14:17], v[186:189], v[66:81]
	v_mfma_f32_32x32x16_f16 v[2:17], v[38:41], v[126:129], 0
	s_nop 10
	v_cvt_pk_f16_f32 v73, v72, v73
	v_cvt_pk_f16_f32 v72, v70, v71
	v_cvt_pk_f16_f32 v70, v66, v67
	v_cvt_pk_f16_f32 v67, v76, v77
	v_cvt_pk_f16_f32 v66, v74, v75
	global_load_dwordx4 v[74:77], v154, s[2:3]
	v_cvt_pk_f16_f32 v71, v68, v69
	v_cvt_pk_f16_f32 v69, v80, v81
	v_cvt_pk_f16_f32 v68, v78, v79
	global_load_dwordx4 v[78:81], v154, s[2:3] offset:1024
	ds_read_b128 v[18:21], v180
	ds_read_b128 v[22:25], v176
	ds_read_b128 v[26:29], v180 offset:32768
	global_load_dwordx4 v[30:33], v154, s[2:3] offset:2048
	v_mfma_f32_32x32x16_f16 v[34:49], v[38:41], v[110:113], 0
	v_mfma_f32_32x32x16_f16 v[2:17], v[82:85], v[122:125], v[2:17]
	v_mfma_f32_32x32x16_f16 v[34:49], v[82:85], v[106:109], v[34:49]
	ds_read_b128 v[82:85], v176 offset:32768
	s_waitcnt vmcnt(2) lgkmcnt(3)
	v_mfma_f32_32x32x16_f16 v[50:65], v[18:21], v[74:77], 0
	v_mfma_f32_32x32x16_f16 v[2:17], v[70:73], v[118:121], v[2:17]
	v_mfma_f32_32x32x16_f16 v[34:49], v[70:73], v[94:97], v[34:49]
	v_lshl_add_u64 v[70:71], s[2:3], 0, v[154:155]
	v_add_co_u32_e32 v152, vcc, s23, v70
	s_nop 1
	v_addc_co_u32_e32 v153, vcc, 0, v71, vcc
	s_waitcnt vmcnt(1) lgkmcnt(2)
	v_mfma_f32_32x32x16_f16 v[50:65], v[22:25], v[78:81], v[50:65]
	v_mfma_f32_32x32x16_f16 v[2:17], v[66:69], v[114:117], v[2:17]
	v_mfma_f32_32x32x16_f16 v[34:49], v[66:69], v[90:93], v[34:49]
	global_load_dwordx4 v[66:69], v154, s[2:3] offset:3072
	s_nop 9
	v_cvt_pk_f16_f32 v9, v8, v9
	v_cvt_pk_f16_f32 v8, v6, v7
	v_cvt_pk_f16_f32 v7, v4, v5
	v_cvt_pk_f16_f32 v6, v2, v3
	v_cvt_pk_f16_f32 v5, v16, v17
	v_cvt_pk_f16_f32 v4, v14, v15
	s_waitcnt vmcnt(1) lgkmcnt(1)
	v_mfma_f32_32x32x16_f16 v[50:65], v[26:29], v[30:33], v[50:65]
	global_load_dwordx4 v[30:33], v168, s[2:3]
	global_load_dwordx4 v[86:89], v[152:153], off offset:1024
	s_nop 0
	global_load_dwordx4 v[168:171], v168, s[0:1]
	v_cvt_pk_f16_f32 v3, v12, v13
	v_cvt_pk_f16_f32 v2, v10, v11
	ds_write_b128 v175, v[6:9]
	ds_write_b128 v174, v[2:5]
	v_cvt_pk_f16_f32 v5, v40, v41
	s_waitcnt vmcnt(3) lgkmcnt(2)
	v_mfma_f32_32x32x16_f16 v[50:65], v[82:85], v[66:69], v[50:65]
	global_load_dwordx4 v[182:185], v154, s[0:1] offset:1024
	v_cvt_pk_f16_f32 v4, v38, v39
	v_cvt_pk_f16_f32 v3, v36, v37
	v_cvt_pk_f16_f32 v2, v34, v35
	ds_write_b128 v175, v[2:5] offset:32768
	v_cvt_pk_f16_f32 v5, v48, v49
	v_cvt_pk_f16_f32 v4, v46, v47
	s_waitcnt vmcnt(3)
	v_mfma_f32_32x32x16_f16 v[66:81], v[18:21], v[30:33], 0
	global_load_dwordx4 v[18:21], v[152:153], off offset:2048
	v_cvt_pk_f16_f32 v3, v44, v45
	v_cvt_pk_f16_f32 v2, v42, v43
	ds_write_b128 v174, v[2:5] offset:32768
	v_cvt_pk_f16_f32 v57, v56, v57
	v_cvt_pk_f16_f32 v56, v54, v55
	v_cvt_pk_f16_f32 v55, v52, v53
	s_waitcnt vmcnt(3)
	v_mfma_f32_32x32x16_f16 v[66:81], v[22:25], v[86:89], v[66:81]
	global_load_dwordx4 v[22:25], v[152:153], off offset:3072
	v_cvt_pk_f16_f32 v54, v50, v51
	s_waitcnt vmcnt(1)
	v_mfma_f32_32x32x16_f16 v[66:81], v[26:29], v[18:21], v[66:81]
	v_lshl_add_u64 v[18:19], s[0:1], 0, v[154:155]
	v_add_co_u32_e32 v152, vcc, s23, v18
	s_nop 1
	v_addc_co_u32_e32 v153, vcc, 0, v19, vcc
	global_load_dwordx4 v[86:89], v[152:153], off offset:1024
	s_waitcnt vmcnt(1)
	v_mfma_f32_32x32x16_f16 v[66:81], v[82:85], v[22:25], v[66:81]
	v_cvt_pk_f16_f32 v85, v64, v65
	v_cvt_pk_f16_f32 v84, v62, v63
	v_cvt_pk_f16_f32 v83, v60, v61
	v_cvt_pk_f16_f32 v82, v58, v59
	v_mfma_f32_32x32x16_f16 v[18:33], v[54:57], v[126:129], 0
	s_nop 6
	v_cvt_pk_f16_f32 v73, v72, v73
	v_cvt_pk_f16_f32 v72, v70, v71
	v_cvt_pk_f16_f32 v70, v66, v67
	v_cvt_pk_f16_f32 v67, v76, v77
	v_cvt_pk_f16_f32 v66, v74, v75
	global_load_dwordx4 v[74:77], v154, s[0:1]
	ds_read_b128 v[2:5], v181
	ds_read_b128 v[6:9], v177
	ds_read_b128 v[10:13], v181 offset:32768
	global_load_dwordx4 v[14:17], v154, s[0:1] offset:2048
	global_load_dwordx4 v[34:37], v154, s[0:1] offset:3072
	v_mfma_f32_32x32x16_f16 v[50:65], v[54:57], v[110:113], 0
	v_cvt_pk_f16_f32 v71, v68, v69
	v_cvt_pk_f16_f32 v69, v80, v81
	v_cvt_pk_f16_f32 v68, v78, v79
	v_mfma_f32_32x32x16_f16 v[18:33], v[82:85], v[122:125], v[18:33]
	v_mfma_f32_32x32x16_f16 v[50:65], v[82:85], v[106:109], v[50:65]
	ds_read_b128 v[82:85], v177 offset:32768
	v_mfma_f32_32x32x16_f16 v[18:33], v[70:73], v[118:121], v[18:33]
	v_mfma_f32_32x32x16_f16 v[50:65], v[70:73], v[94:97], v[50:65]
	v_mfma_f32_32x32x16_f16 v[18:33], v[66:69], v[114:117], v[18:33]
	v_mfma_f32_32x32x16_f16 v[50:65], v[66:69], v[90:93], v[50:65]
	s_nop 10
	v_cvt_pk_f16_f32 v25, v24, v25
	v_cvt_pk_f16_f32 v24, v22, v23
	v_cvt_pk_f16_f32 v23, v20, v21
	v_cvt_pk_f16_f32 v22, v18, v19
	ds_write_b128 v132, v[22:25]
	s_waitcnt vmcnt(2) lgkmcnt(4)
	v_mfma_f32_32x32x16_f16 v[66:81], v[2:5], v[74:77], 0
	s_waitcnt lgkmcnt(3)
	v_mfma_f32_32x32x16_f16 v[66:81], v[6:9], v[182:185], v[66:81]
	s_waitcnt vmcnt(1) lgkmcnt(2)
	v_mfma_f32_32x32x16_f16 v[66:81], v[10:13], v[14:17], v[66:81]
	s_waitcnt vmcnt(0) lgkmcnt(1)
	v_mfma_f32_32x32x16_f16 v[66:81], v[82:85], v[34:37], v[66:81]
	v_mfma_f32_32x32x16_f16 v[34:49], v[2:5], v[168:171], 0
	global_load_dwordx4 v[2:5], v[152:153], off offset:2048
	s_nop 9
	v_cvt_pk_f16_f32 v73, v72, v73
	v_cvt_pk_f16_f32 v72, v70, v71
	v_cvt_pk_f16_f32 v71, v68, v69
	v_cvt_pk_f16_f32 v70, v66, v67
	v_cvt_pk_f16_f32 v69, v80, v81
	v_cvt_pk_f16_f32 v68, v78, v79
	v_mfma_f32_32x32x16_f16 v[34:49], v[6:9], v[86:89], v[34:49]
	global_load_dwordx4 v[6:9], v[152:153], off offset:3072
	v_cvt_pk_f16_f32 v67, v76, v77
	v_cvt_pk_f16_f32 v66, v74, v75
	s_waitcnt vmcnt(1)
	v_mfma_f32_32x32x16_f16 v[34:49], v[10:13], v[2:5], v[34:49]
	s_waitcnt vmcnt(0)
	v_mfma_f32_32x32x16_f16 v[34:49], v[82:85], v[6:9], v[34:49]
	v_mfma_f32_32x32x16_f16 v[2:17], v[70:73], v[126:129], 0
	s_nop 10
	v_cvt_pk_f16_f32 v41, v40, v41
	v_cvt_pk_f16_f32 v40, v38, v39
	v_cvt_pk_f16_f32 v38, v34, v35
	v_cvt_pk_f16_f32 v35, v44, v45
	v_cvt_pk_f16_f32 v34, v42, v43
	v_cvt_pk_f16_f32 v45, v32, v33
	v_cvt_pk_f16_f32 v44, v30, v31
	v_cvt_pk_f16_f32 v43, v28, v29
	v_cvt_pk_f16_f32 v42, v26, v27
	v_mfma_f32_32x32x16_f16 v[18:33], v[70:73], v[110:113], 0
	v_cvt_pk_f16_f32 v39, v36, v37
	v_cvt_pk_f16_f32 v37, v48, v49
	v_cvt_pk_f16_f32 v36, v46, v47
	ds_write_b128 v131, v[42:45]
	v_cvt_pk_f16_f32 v45, v56, v57
	v_cvt_pk_f16_f32 v44, v54, v55
	v_cvt_pk_f16_f32 v43, v52, v53
	v_mfma_f32_32x32x16_f16 v[2:17], v[66:69], v[122:125], v[2:17]
	v_cvt_pk_f16_f32 v42, v50, v51
	ds_write_b128 v132, v[42:45] offset:32768
	v_cvt_pk_f16_f32 v45, v64, v65
	v_cvt_pk_f16_f32 v44, v62, v63
	v_cvt_pk_f16_f32 v43, v60, v61
	v_cvt_pk_f16_f32 v42, v58, v59
	ds_write_b128 v131, v[42:45] offset:32768
	v_mfma_f32_32x32x16_f16 v[18:33], v[66:69], v[106:109], v[18:33]
	v_mfma_f32_32x32x16_f16 v[2:17], v[38:41], v[118:121], v[2:17]
	v_mfma_f32_32x32x16_f16 v[18:33], v[38:41], v[94:97], v[18:33]
	v_mfma_f32_32x32x16_f16 v[2:17], v[34:37], v[114:117], v[2:17]
	v_mfma_f32_32x32x16_f16 v[18:33], v[34:37], v[90:93], v[18:33]
	s_nop 10
	v_cvt_pk_f16_f32 v9, v8, v9
	v_cvt_pk_f16_f32 v8, v6, v7
	v_cvt_pk_f16_f32 v7, v4, v5
	v_cvt_pk_f16_f32 v6, v2, v3
	v_cvt_pk_f16_f32 v5, v16, v17
	v_cvt_pk_f16_f32 v4, v14, v15
	v_cvt_pk_f16_f32 v3, v12, v13
	v_cvt_pk_f16_f32 v2, v10, v11
	ds_write_b128 v135, v[6:9]
	ds_write_b128 v133, v[2:5]
	v_cvt_pk_f16_f32 v5, v24, v25
	v_cvt_pk_f16_f32 v4, v22, v23
	v_cvt_pk_f16_f32 v3, v20, v21
	v_cvt_pk_f16_f32 v2, v18, v19
	ds_write_b128 v135, v[2:5] offset:32768
	v_cvt_pk_f16_f32 v5, v32, v33
	v_cvt_pk_f16_f32 v4, v30, v31
	v_cvt_pk_f16_f32 v3, v28, v29
	v_cvt_pk_f16_f32 v2, v26, v27
	ds_write_b128 v133, v[2:5] offset:32768
	s_setprio 0
	s_waitcnt lgkmcnt(0)
	s_barrier
	s_cmp_lt_i32 s22, 0
	s_cbranch_scc0 .Lno_pref
	s_add_u32 s36, s10, 0x140000
	s_addc_u32 s37, s11, 0
	v_lshlrev_b32_e32 v192, 3, v156
	v_lshlrev_b32_e32 v193, 3, v167
	global_load_dwordx2 v[190:191], v192, s[36:37]
	global_load_dwordx2 v[194:195], v193, s[36:37] offset:2048
